# hybrid K1 ring 32 + queue flush spread over the stream (slot atomics issued at every chunk boundary instead of one burst at wave end)
# speedup vs baseline: 1.0505x; 1.0134x over previous
.Lk1_scan:
	s_load_dwordx2 s[4:5], s[0:1], 0x0
	s_load_dwordx4 s[8:11], s[0:1], 0x20
	s_load_dwordx2 s[12:13], s[0:1], 0x30
	v_and_b32_e32 v6, 63, v0
	v_readfirstlane_b32 s3, v0
	v_lshlrev_b32_e32 v1, 4, v6
	v_lshlrev_b32_e32 v2, 2, v6
	v_or_b32_e32 v3, 1, v2
	v_or_b32_e32 v4, 2, v2
	v_or_b32_e32 v5, 3, v2
	s_lshr_b32 s3, s3, 6
	s_sub_u32 s16, s2, 0x60
	s_lshl_b32 s16, s16, 2
	s_add_u32 s16, s16, s3
	s_mul_i32 s17, s16, 0x48000
	s_lshr_b32 s18, s17, 2
	s_lshl_b32 s24, s3, 13
	s_mov_b32 s25, s24
	s_mov_b32 s28, s24
	s_mov_b32 s36, 0
	v_mov_b32_e32 v21, 1
	s_mov_b32 s27, 0
	s_mov_b32 s29, 0x55555556
	s_mov_b32 s31, 0xc0000
	s_waitcnt lgkmcnt(0)
	s_and_b32 s50, s16, 15
	s_mul_i32 s52, s50, 256
	s_add_u32 s52, s52, 14336
	s_lshl_b32 s53, s50, 6
	s_add_u32 s53, s53, 0xe000
	s_add_u32 s54, s10, s53
	s_addc_u32 s55, s11, 0
	s_mul_i32 s59, s16, 7
	s_mul_i32 s57, s59, 0x8000
	s_lshr_b32 s18, s57, 2
	s_add_u32 s6, s4, s57
	s_addc_u32 s7, s5, 0
	v_mov_b32_e32 v27, 0
	global_load_dwordx4 v[28:31], v1, s[6:7] nt
	s_add_u32 s6, s6, 0x400
	s_addc_u32 s7, s7, 0
	global_load_dwordx4 v[32:35], v1, s[6:7] nt
	s_add_u32 s6, s6, 0x400
	s_addc_u32 s7, s7, 0
	global_load_dwordx4 v[36:39], v1, s[6:7] nt
	s_add_u32 s6, s6, 0x400
	s_addc_u32 s7, s7, 0
	global_load_dwordx4 v[40:43], v1, s[6:7] nt
	s_add_u32 s6, s6, 0x400
	s_addc_u32 s7, s7, 0
	global_load_dwordx4 v[44:47], v1, s[6:7] nt
	s_add_u32 s6, s6, 0x400
	s_addc_u32 s7, s7, 0
	global_load_dwordx4 v[48:51], v1, s[6:7] nt
	s_add_u32 s6, s6, 0x400
	s_addc_u32 s7, s7, 0
	global_load_dwordx4 v[52:55], v1, s[6:7] nt
	s_add_u32 s6, s6, 0x400
	s_addc_u32 s7, s7, 0
	global_load_dwordx4 v[56:59], v1, s[6:7] nt
	s_add_u32 s6, s6, 0x400
	s_addc_u32 s7, s7, 0
	global_load_dwordx4 v[60:63], v1, s[6:7] nt
	s_add_u32 s6, s6, 0x400
	s_addc_u32 s7, s7, 0
	global_load_dwordx4 v[64:67], v1, s[6:7] nt
	s_add_u32 s6, s6, 0x400
	s_addc_u32 s7, s7, 0
	global_load_dwordx4 v[68:71], v1, s[6:7] nt
	s_add_u32 s6, s6, 0x400
	s_addc_u32 s7, s7, 0
	global_load_dwordx4 v[72:75], v1, s[6:7] nt
	s_add_u32 s6, s6, 0x400
	s_addc_u32 s7, s7, 0
	global_load_dwordx4 v[76:79], v1, s[6:7] nt
	s_add_u32 s6, s6, 0x400
	s_addc_u32 s7, s7, 0
	global_load_dwordx4 v[80:83], v1, s[6:7] nt
	s_add_u32 s6, s6, 0x400
	s_addc_u32 s7, s7, 0
	global_load_dwordx4 v[84:87], v1, s[6:7] nt
	s_add_u32 s6, s6, 0x400
	s_addc_u32 s7, s7, 0
	global_load_dwordx4 v[88:91], v1, s[6:7] nt
	s_add_u32 s6, s6, 0x400
	s_addc_u32 s7, s7, 0
	global_load_dwordx4 v[92:95], v1, s[6:7] nt
	s_add_u32 s6, s6, 0x400
	s_addc_u32 s7, s7, 0
	global_load_dwordx4 v[96:99], v1, s[6:7] nt
	s_add_u32 s6, s6, 0x400
	s_addc_u32 s7, s7, 0
	global_load_dwordx4 v[100:103], v1, s[6:7] nt
	s_add_u32 s6, s6, 0x400
	s_addc_u32 s7, s7, 0
	global_load_dwordx4 v[104:107], v1, s[6:7] nt
	s_add_u32 s6, s6, 0x400
	s_addc_u32 s7, s7, 0
	global_load_dwordx4 v[108:111], v1, s[6:7] nt
	s_add_u32 s6, s6, 0x400
	s_addc_u32 s7, s7, 0
	global_load_dwordx4 v[112:115], v1, s[6:7] nt
	s_add_u32 s6, s6, 0x400
	s_addc_u32 s7, s7, 0
	global_load_dwordx4 v[116:119], v1, s[6:7] nt
	s_add_u32 s6, s6, 0x400
	s_addc_u32 s7, s7, 0
	global_load_dwordx4 v[120:123], v1, s[6:7] nt
	s_add_u32 s6, s6, 0x400
	s_addc_u32 s7, s7, 0
	global_load_dwordx4 v[124:127], v1, s[6:7] nt
	s_add_u32 s6, s6, 0x400
	s_addc_u32 s7, s7, 0
	global_load_dwordx4 v[128:131], v1, s[6:7] nt
	s_add_u32 s6, s6, 0x400
	s_addc_u32 s7, s7, 0
	global_load_dwordx4 v[132:135], v1, s[6:7] nt
	s_add_u32 s6, s6, 0x400
	s_addc_u32 s7, s7, 0
	global_load_dwordx4 v[136:139], v1, s[6:7] nt
	s_add_u32 s6, s6, 0x400
	s_addc_u32 s7, s7, 0
	global_load_dwordx4 v[140:143], v1, s[6:7] nt
	s_add_u32 s6, s6, 0x400
	s_addc_u32 s7, s7, 0
	global_load_dwordx4 v[144:147], v1, s[6:7] nt
	s_add_u32 s6, s6, 0x400
	s_addc_u32 s7, s7, 0
	global_load_dwordx4 v[148:151], v1, s[6:7] nt
	s_add_u32 s6, s6, 0x400
	s_addc_u32 s7, s7, 0
	global_load_dwordx4 v[152:155], v1, s[6:7] nt
	s_add_u32 s6, s6, 0x400
	s_addc_u32 s7, s7, 0
	s_mov_b32 s26, 9
	s_add_u32 s57, s59, 1
	s_mul_i32 s57, s57, 0x8000
	s_lshr_b32 s58, s57, 2
	s_add_u32 s6, s4, s57
	s_addc_u32 s7, s5, 0
	s_mov_b32 s26, 0
.Lk1_main:
	s_cmp_eq_u32 s36, 0
	s_cbranch_scc1 .Lk1_cskip_m
	s_mov_b64 exec, s[34:35]
	v_mul_u32_u24_e32 v24, 0x3000, v19
	v_lshlrev_b32_e32 v23, 6, v19
	v_cmp_gt_u32_e32 vcc, 64, v22
	v_add_u32_e32 v23, v23, v22
	v_add3_u32 v24, v24, v22, s31
	v_cndmask_b32_e32 v23, v24, v23, vcc
	v_lshlrev_b32_e32 v23, 3, v23
	global_store_dwordx2 v23, v[16:17], s[12:13]
	s_mov_b64 exec, -1
	s_mov_b32 s36, 0
.Lk1_cskip_m:
	s_cmp_ge_u32 s28, s25
	s_cbranch_scc1 .Lk1_inone_m
	s_waitcnt lgkmcnt(0)
	v_lshl_add_u32 v25, v6, 3, s28
	v_cmp_gt_u32_e32 vcc, s25, v25
	s_and_saveexec_b64 s[32:33], vcc
	s_mov_b64 s[34:35], exec
	ds_read_b64 v[16:17], v25
	s_waitcnt lgkmcnt(0)
	v_lshrrev_b32_e32 v23, 12, v16
	v_mul_hi_u32 v23, v23, s29
	v_mul_u32_u24_e32 v19, 0x3000, v23
	v_sub_u32_e32 v19, v16, v19
	v_lshlrev_b32_e32 v20, 2, v19
	global_atomic_add v22, v20, v21, s[8:9] sc0
	global_atomic_add_f32 v20, v17, s[10:11]
	v_mov_b32_e32 v16, v23
	s_mov_b64 exec, -1
	s_mov_b32 s36, 1
	s_add_u32 s28, s28, 0x200
	s_cmp_ge_u32 s28, s25
	s_cbranch_scc0 .Lk1_inone_m
	s_mov_b32 s28, s24
	s_mov_b32 s25, s24

.Lk1_noreq:
	s_add_u32 s26, s26, 1
	s_branch .Lk1_main
.Lk1_lastchunk:
	s_cmp_eq_u32 s36, 0
	s_cbranch_scc1 .Lk1_cskip_l
	s_mov_b64 exec, s[34:35]
	v_mul_u32_u24_e32 v24, 0x3000, v19
	v_lshlrev_b32_e32 v23, 6, v19
	v_cmp_gt_u32_e32 vcc, 64, v22
	v_add_u32_e32 v23, v23, v22
	v_add3_u32 v24, v24, v22, s31
	v_cndmask_b32_e32 v23, v24, v23, vcc
	v_lshlrev_b32_e32 v23, 3, v23
	global_store_dwordx2 v23, v[16:17], s[12:13]
	s_mov_b64 exec, -1
	s_mov_b32 s36, 0
